# speedup vs baseline: 1.0324x; 1.0324x over previous
_Z9gemm_gldsILi256ELi192ELi4ELi2ELi2ELi4ELi8ELi0ELi4096ELi3072ELi1024EEvPKDF16_S1_PfPKfS4_PKiPDF16_S7_S7_:
	s_ashr_i32 s3, s2, 3
	s_lshr_b32 s9, s3, 30
	s_add_i32 s9, s3, s9
	s_lshl_b32 s8, s2, 1
	s_ashr_i32 s10, s9, 2
	s_and_b32 s9, s9, 0xfffffc
	s_lshl_b32 s2, s2, 3
	s_load_dwordx4 s[4:7], s[0:1], 0x0
	s_and_b32 s8, s8, 12
	s_sub_i32 s3, s3, s9
	s_and_b32 s20, s2, 8
	s_add_i32 s8, s8, s3
	s_add_i32 s20, s20, s10
	s_lshl_b32 s16, s8, 8
	s_mul_i32 s2, s20, 0xc0
	v_lshlrev_b32_e32 v139, 4, v0
	v_and_b32_e32 v1, 32, v0
	s_ashr_i32 s17, s16, 31
	s_ashr_i32 s3, s2, 31
	v_lshrrev_b32_e32 v2, 3, v0
	v_bfe_u32 v46, v0, 2, 4
	v_bitop3_b32 v1, v139, v1, 48 bitop3:0x6c
	s_lshl_b64 s[8:9], s[16:17], 11
	s_lshl_b64 s[10:11], s[2:3], 11
	v_and_or_b32 v2, v2, 48, v46
	v_and_or_b32 v47, v0, 64, v1
	s_waitcnt lgkmcnt(0)
	s_add_u32 s2, s4, s8
	s_addc_u32 s3, s5, s9
	v_lshl_or_b32 v2, v2, 11, v47
	v_mov_b32_e32 v3, 0
	v_readfirstlane_b32 s4, v139
	v_or_b32_e32 v1, 0x2000, v139
	s_add_u32 s18, s6, s10
	v_lshl_add_u64 v[4:5], s[2:3], 0, v[2:3]
	s_mov_b32 m0, s4
	s_mov_b64 s[4:5], 0x20000
	v_readfirstlane_b32 s6, v1
	v_or_b32_e32 v1, 0x4000, v139
	s_addc_u32 s19, s7, s11
	global_load_lds_dwordx4 v2, s[2:3]
	v_lshl_add_u64 v[8:9], v[4:5], 0, s[4:5]
	s_mov_b32 m0, s6
	s_mov_b64 s[6:7], 0x40000
	v_readfirstlane_b32 s8, v1
	global_load_lds_dwordx4 v[8:9], off
	v_lshl_add_u64 v[8:9], v[4:5], 0, s[6:7]
	s_mov_b32 m0, s8
	s_mov_b64 s[8:9], 0x60000
	v_or_b32_e32 v1, 0x6000, v139
	global_load_lds_dwordx4 v[8:9], off
	v_lshl_add_u64 v[8:9], v[4:5], 0, s[8:9]
	v_readfirstlane_b32 s8, v1
	v_or_b32_e32 v1, 0x8000, v139
	v_lshl_add_u64 v[6:7], s[18:19], 0, v[2:3]
	s_mov_b32 m0, s8
	v_readfirstlane_b32 s8, v1
	v_or_b32_e32 v1, 0xa000, v139
	global_load_lds_dwordx4 v[8:9], off
	s_mov_b32 m0, s8
	v_lshl_add_u64 v[8:9], v[6:7], 0, s[4:5]
	v_readfirstlane_b32 s4, v1
	v_or_b32_e32 v1, 0xc000, v139
	global_load_lds_dwordx4 v2, s[18:19]
	s_mov_b32 m0, s4
	v_readfirstlane_b32 s4, v1
	v_or_b32_e32 v1, 0xe000, v139
	global_load_lds_dwordx4 v[8:9], off
	v_lshl_add_u64 v[8:9], v[6:7], 0, s[6:7]
	s_mov_b32 m0, s4
	s_mov_b64 s[4:5], 0x80
	v_readfirstlane_b32 s6, v1
	v_or_b32_e32 v1, 0x10000, v139
	global_load_lds_dwordx4 v[8:9], off
	v_lshl_add_u64 v[8:9], v[4:5], 0, s[4:5]
	s_mov_b32 m0, s6
	s_mov_b64 s[6:7], 0x20080
	v_readfirstlane_b32 s8, v1
	v_or_b32_e32 v1, 0x12000, v139
	global_load_lds_dwordx4 v[8:9], off
	v_lshl_add_u64 v[8:9], v[4:5], 0, s[6:7]
	s_mov_b32 m0, s8
	v_readfirstlane_b32 s10, v1
	global_load_lds_dwordx4 v[8:9], off
	s_mov_b64 s[8:9], 0x40080
	s_mov_b32 m0, s10
	s_mov_b64 s[10:11], 0x60080
	v_or_b32_e32 v1, 0x14000, v139
	v_lshl_add_u64 v[8:9], v[4:5], 0, s[8:9]
	v_lshl_add_u64 v[4:5], v[4:5], 0, s[10:11]
	v_readfirstlane_b32 s10, v1
	global_load_lds_dwordx4 v[8:9], off
	s_mov_b32 m0, s10
	v_or_b32_e32 v1, 0x16000, v139
	global_load_lds_dwordx4 v[4:5], off
	v_lshl_add_u64 v[4:5], v[6:7], 0, s[4:5]
	v_readfirstlane_b32 s4, v1
	v_or_b32_e32 v1, 0x18000, v139
	s_mov_b32 m0, s4
	v_readfirstlane_b32 s4, v1
	v_or_b32_e32 v1, 0x1a000, v139
	global_load_lds_dwordx4 v[4:5], off
	v_lshl_add_u64 v[4:5], v[6:7], 0, s[6:7]
	s_mov_b32 m0, s4
	v_readfirstlane_b32 s4, v1
	global_load_lds_dwordx4 v[4:5], off
	v_lshl_add_u64 v[4:5], v[6:7], 0, s[8:9]
	s_mov_b32 m0, s4
	v_lshrrev_b32_e32 v2, 7, v0
	global_load_lds_dwordx4 v[4:5], off
	s_load_dwordx4 s[12:15], s[0:1], 0x38
	s_load_dwordx8 s[4:11], s[0:1], 0x18
	v_lshlrev_b32_e32 v4, 6, v0
	v_and_b32_e32 v138, 48, v0
	v_and_b32_e32 v4, 0x3c0, v4
	v_lshlrev_b32_e32 v6, 2, v0
	v_bfe_u32 v144, v0, 6, 1
	v_or_b32_e32 v14, v4, v138
	v_lshlrev_b32_e32 v5, 13, v2
	v_and_b32_e32 v15, 32, v6
	v_and_b32_e32 v1, 15, v0
	v_bitop3_b32 v151, v4, v15, v138 bitop3:0x36
	v_bitop3_b32 v146, v5, v14, v15 bitop3:0xf6
	v_mul_u32_u24_e32 v152, 0x3000, v144
	v_lshl_or_b32 v145, v2, 6, s16
	v_or_b32_e32 v4, v145, v1
	v_ashrrev_i32_e32 v5, 31, v4
	s_waitcnt lgkmcnt(0)
	v_lshl_add_u64 v[4:5], v[4:5], 2, s[8:9]
	global_load_dword v150, v[4:5], off
	global_load_dword v149, v[4:5], off offset:64
	global_load_dword v148, v[4:5], off offset:128
	global_load_dword v147, v[4:5], off offset:192
	v_bitop3_b32 v153, v152, v14, v15 bitop3:0xf6
	v_mov_b32_e32 v48, v3
	v_mov_b32_e32 v49, v3
	v_mov_b32_e32 v50, v3
	v_mov_b32_e32 v51, v3
	v_mov_b32_e32 v52, v3
	v_mov_b32_e32 v53, v3
	v_mov_b32_e32 v54, v3
	v_mov_b32_e32 v55, v3
	v_mov_b32_e32 v56, v3
	v_mov_b32_e32 v57, v3
	v_mov_b32_e32 v58, v3
	v_mov_b32_e32 v59, v3
	v_mov_b32_e32 v60, v3
	v_mov_b32_e32 v61, v3
	v_mov_b32_e32 v62, v3
	v_mov_b32_e32 v63, v3
	v_mov_b32_e32 v64, v3
	v_mov_b32_e32 v65, v3
	v_mov_b32_e32 v66, v3
	v_mov_b32_e32 v67, v3
	v_mov_b32_e32 v68, v3
	v_mov_b32_e32 v69, v3
	v_mov_b32_e32 v70, v3
	v_mov_b32_e32 v71, v3
	v_mov_b32_e32 v72, v3
	v_mov_b32_e32 v73, v3
	v_mov_b32_e32 v74, v3
	v_mov_b32_e32 v75, v3
	v_mov_b32_e32 v76, v3
	v_mov_b32_e32 v77, v3
	v_mov_b32_e32 v86, v3
	v_mov_b32_e32 v87, v3
	v_mov_b32_e32 v88, v3
	v_mov_b32_e32 v89, v3
	v_mov_b32_e32 v98, v3
	v_mov_b32_e32 v99, v3
	v_mov_b32_e32 v100, v3
	v_mov_b32_e32 v101, v3
	v_mov_b32_e32 v130, v3
	v_mov_b32_e32 v131, v3
	v_mov_b32_e32 v132, v3
	v_mov_b32_e32 v133, v3
	v_mov_b32_e32 v78, v3
	v_mov_b32_e32 v79, v3
	v_mov_b32_e32 v80, v3
	v_mov_b32_e32 v81, v3
	v_mov_b32_e32 v82, v3
	v_mov_b32_e32 v83, v3
	v_mov_b32_e32 v84, v3
	v_mov_b32_e32 v85, v3
	v_mov_b32_e32 v90, v3
	v_mov_b32_e32 v91, v3
	v_mov_b32_e32 v92, v3
	v_mov_b32_e32 v93, v3
	v_mov_b32_e32 v94, v3
	v_mov_b32_e32 v95, v3
	v_mov_b32_e32 v96, v3
	v_mov_b32_e32 v97, v3
	v_mov_b32_e32 v102, v3
	v_mov_b32_e32 v103, v3
	v_mov_b32_e32 v104, v3
	v_mov_b32_e32 v105, v3
	v_mov_b32_e32 v106, v3
	v_mov_b32_e32 v107, v3
	v_mov_b32_e32 v108, v3
	v_mov_b32_e32 v109, v3
	v_mov_b32_e32 v110, v3
	v_mov_b32_e32 v111, v3
	v_mov_b32_e32 v112, v3
	v_mov_b32_e32 v113, v3
	v_mov_b32_e32 v114, v3
	v_mov_b32_e32 v115, v3
	v_mov_b32_e32 v116, v3
	v_mov_b32_e32 v117, v3
	v_mov_b32_e32 v118, v3
	v_mov_b32_e32 v119, v3
	v_mov_b32_e32 v120, v3
	v_mov_b32_e32 v121, v3
	v_mov_b32_e32 v122, v3
	v_mov_b32_e32 v123, v3
	v_mov_b32_e32 v124, v3
	v_mov_b32_e32 v125, v3
	v_mov_b32_e32 v134, v3
	v_mov_b32_e32 v135, v3
	v_mov_b32_e32 v136, v3
	v_mov_b32_e32 v137, v3
	v_mov_b32_e32 v126, v3
	v_mov_b32_e32 v127, v3
	v_mov_b32_e32 v128, v3
	v_mov_b32_e32 v129, v3
	s_waitcnt vmcnt(7) lgkmcnt(0)
	s_barrier
	ds_read_b128 v[42:45], v146
	ds_read_b128 v[38:41], v146 offset:2048
	ds_read_b128 v[10:13], v146 offset:4096
	ds_read_b128 v[6:9], v146 offset:6144
	ds_read_b128 v[22:25], v153 offset:32768
	ds_read_b128 v[18:21], v153 offset:34816
	ds_read_b128 v[30:33], v153 offset:36864
	ds_read_b128 v[26:29], v153 offset:38912
	ds_read_b128 v[34:37], v153 offset:40960
	ds_read_b128 v[14:17], v153 offset:43008
	v_lshl_or_b32 v2, v2, 15, v47
	v_lshl_or_b32 v2, v46, 11, v2
	v_lshl_add_u64 v[140:141], s[18:19], 0, v[2:3]
	v_lshl_add_u64 v[142:143], s[2:3], 0, v[2:3]
	s_mov_b32 s21, 0
	s_mov_b64 s[0:1], 0
	s_mov_b64 s[2:3], 0x100
	s_mov_b64 s[8:9], 0x20100
	s_mov_b64 s[16:17], 0x40100
	s_mov_b64 s[18:19], 0x60100
	v_mov_b32_e32 v2, v3
	v_mov_b32_e32 v4, v3
	v_mov_b32_e32 v5, v3
	v_mov_b32_e32 v46, v3
	v_mov_b32_e32 v47, v3

_Z9gemm_gldsILi128ELi128ELi4ELi2ELi3ELi8ELi4ELi1ELi4096ELi1024ELi1024EEvPKDF16_S1_PfPKfS4_PKiPDF16_S7_S7_:
	s_load_dwordx4 s[4:7], s[0:1], 0x0
	s_load_dwordx2 s[8:9], s[0:1], 0x10
	s_ashr_i32 s0, s2, 3
	s_lshr_b32 s3, s0, 29
	s_add_i32 s3, s0, s3
	s_lshl_b32 s1, s2, 2
	s_lshr_b32 s10, s3, 3
	s_and_b32 s3, s3, 0x1fffff8
	s_and_b32 s2, s1, 24
	s_sub_i32 s0, s0, s3
	s_add_i32 s2, s2, s0
	s_and_b32 s0, s1, 4
	s_add_i32 s0, s0, s10
	s_lshl_b32 s2, s2, 7
	s_lshl_b32 s0, s0, 7
	v_lshlrev_b32_e32 v66, 4, v0
	v_and_b32_e32 v1, 32, v0
	s_ashr_i32 s3, s2, 31
	s_ashr_i32 s1, s0, 31
	v_lshrrev_b32_e32 v2, 3, v0
	v_bfe_u32 v30, v0, 2, 4
	v_bitop3_b32 v1, v66, v1, 48 bitop3:0x6c
	s_lshl_b64 s[10:11], s[2:3], 11
	s_lshl_b64 s[12:13], s[0:1], 11
	v_and_or_b32 v2, v2, 48, v30
	v_and_or_b32 v31, v0, 64, v1
	s_waitcnt lgkmcnt(0)
	s_add_u32 s4, s4, s10
	s_addc_u32 s5, s5, s11
	v_lshl_or_b32 v2, v2, 11, v31
	v_mov_b32_e32 v3, 0
	v_readfirstlane_b32 s3, v66
	v_or_b32_e32 v1, 0x2000, v66
	s_add_u32 s6, s6, s12
	v_lshl_add_u64 v[4:5], s[4:5], 0, v[2:3]
	s_mov_b32 m0, s3
	s_mov_b64 s[10:11], 0x20000
	v_readfirstlane_b32 s3, v1
	v_or_b32_e32 v1, 0x4000, v66
	s_addc_u32 s7, s7, s13
	global_load_lds_dwordx4 v2, s[4:5]
	v_lshl_add_u64 v[8:9], v[4:5], 0, s[10:11]
	s_mov_b32 m0, s3
	v_readfirstlane_b32 s3, v1
	v_or_b32_e32 v1, 0x6000, v66
	v_lshl_add_u64 v[6:7], s[6:7], 0, v[2:3]
	global_load_lds_dwordx4 v[8:9], off
	s_mov_b32 m0, s3
	v_readfirstlane_b32 s3, v1
	v_or_b32_e32 v1, 0x8000, v66
	global_load_lds_dwordx4 v2, s[6:7]
	v_lshl_add_u64 v[8:9], v[6:7], 0, s[10:11]
	s_mov_b32 m0, s3
	s_mov_b64 s[10:11], 0x80
	v_readfirstlane_b32 s3, v1
	v_or_b32_e32 v1, 0xa000, v66
	global_load_lds_dwordx4 v[8:9], off
	v_lshl_add_u64 v[8:9], v[4:5], 0, s[10:11]
	s_mov_b32 m0, s3
	s_mov_b64 s[12:13], 0x20080
	v_readfirstlane_b32 s3, v1
	v_or_b32_e32 v1, 0xc000, v66
	global_load_lds_dwordx4 v[8:9], off
	v_lshl_add_u64 v[8:9], v[4:5], 0, s[12:13]
	s_mov_b32 m0, s3
	v_readfirstlane_b32 s3, v1
	v_or_b32_e32 v1, 0xe000, v66
	global_load_lds_dwordx4 v[8:9], off
	v_lshl_add_u64 v[8:9], v[6:7], 0, s[10:11]
	s_mov_b32 m0, s3
	v_readfirstlane_b32 s3, v1
	v_or_b32_e32 v1, 0x10000, v66
	global_load_lds_dwordx4 v[8:9], off
	v_lshl_add_u64 v[8:9], v[6:7], 0, s[12:13]
	s_mov_b32 m0, s3
	s_mov_b64 s[10:11], 0x100
	v_readfirstlane_b32 s3, v1
	v_or_b32_e32 v1, 0x12000, v66
	global_load_lds_dwordx4 v[8:9], off
	v_lshl_add_u64 v[8:9], v[4:5], 0, s[10:11]
	s_mov_b32 m0, s3
	s_mov_b64 s[12:13], 0x20100
	v_readfirstlane_b32 s3, v1
	v_or_b32_e32 v1, 0x14000, v66
	global_load_lds_dwordx4 v[8:9], off
	v_lshl_add_u64 v[4:5], v[4:5], 0, s[12:13]
	s_mov_b32 m0, s3
	v_readfirstlane_b32 s3, v1
	v_or_b32_e32 v1, 0x16000, v66
	global_load_lds_dwordx4 v[4:5], off
	v_lshl_add_u64 v[4:5], v[6:7], 0, s[10:11]
	s_mov_b32 m0, s3
	v_readfirstlane_b32 s3, v1
	global_load_lds_dwordx4 v[4:5], off
	v_lshl_add_u64 v[4:5], v[6:7], 0, s[12:13]
	s_mov_b32 m0, s3
	v_lshrrev_b32_e32 v63, 7, v0
	global_load_lds_dwordx4 v[4:5], off
	v_and_b32_e32 v2, 48, v0
	v_lshlrev_b32_e32 v4, 6, v0
	s_movk_i32 s3, 0x3c0
	v_lshlrev_b32_e32 v5, 2, v0
	v_bfe_u32 v62, v0, 6, 1
	v_and_or_b32 v2, v4, s3, v2
	v_lshlrev_b32_e32 v4, 12, v63
	v_and_b32_e32 v5, 32, v5
	v_bitop3_b32 v65, v4, v2, v5 bitop3:0xf6
	v_lshlrev_b32_e32 v4, 13, v62
	v_lshrrev_b32_e32 v1, 2, v0
	v_bitop3_b32 v64, v4, v2, v5 bitop3:0xf6
	v_mov_b32_e32 v32, v3
	v_mov_b32_e32 v33, v3
	v_mov_b32_e32 v34, v3
	v_mov_b32_e32 v35, v3
	v_mov_b32_e32 v36, v3
	v_mov_b32_e32 v37, v3
	v_mov_b32_e32 v38, v3
	v_mov_b32_e32 v39, v3
	v_mov_b32_e32 v40, v3
	v_mov_b32_e32 v41, v3
	v_mov_b32_e32 v42, v3
	v_mov_b32_e32 v43, v3
	v_mov_b32_e32 v44, v3
	v_mov_b32_e32 v45, v3
	v_mov_b32_e32 v46, v3
	v_mov_b32_e32 v47, v3
	v_mov_b32_e32 v48, v3
	v_mov_b32_e32 v49, v3
	v_mov_b32_e32 v50, v3
	v_mov_b32_e32 v51, v3
	v_mov_b32_e32 v52, v3
	v_mov_b32_e32 v53, v3
	v_mov_b32_e32 v54, v3
	v_mov_b32_e32 v55, v3
	v_mov_b32_e32 v56, v3
	v_mov_b32_e32 v57, v3
	s_waitcnt vmcnt(8) lgkmcnt(0)
	s_barrier
	ds_read_b128 v[10:13], v65
	ds_read_b128 v[6:9], v65 offset:2048
	ds_read_b128 v[22:25], v64 offset:16384
	ds_read_b128 v[18:21], v64 offset:18432
	ds_read_b128 v[26:29], v64 offset:20480
	ds_read_b128 v[14:17], v64 offset:22528
	v_lshl_or_b32 v2, v63, 15, v31
	v_lshl_or_b32 v2, v30, 11, v2
	v_lshl_add_u64 v[58:59], s[6:7], 0, v[2:3]
	v_lshl_add_u64 v[60:61], s[4:5], 0, v[2:3]
	s_mov_b32 s3, 0
	s_mov_b64 s[4:5], 0
	s_mov_b64 s[6:7], 0x180
	s_mov_b64 s[10:11], 0x20180
	v_mov_b32_e32 v2, v3
	v_mov_b32_e32 v4, v3
	v_mov_b32_e32 v5, v3
	v_mov_b32_e32 v30, v3
	v_mov_b32_e32 v31, v3
